# speedup vs baseline: 1.0028x; 1.0028x over previous
.LBB3_4:
	s_or_b64 exec, exec, s[8:9]
	v_and_b32_e32 v96, 15, v0
	s_and_b32 s4, s35, 6
	v_mad_u64_u32 v[98:99], s[4:5], s4, 51, v[96:97]
	v_lshrrev_b32_e32 v108, 4, v0
	v_bfe_u32 v99, v0, 4, 2
	s_and_b32 s11, s34, 64
	v_and_b32_e32 v0, 6, v0
	v_or_b32_e32 v1, s11, v96
	v_bitop3_b32 v0, v108, v0, 3 bitop3:0x6c
	v_lshlrev_b32_e32 v1, 7, v1
	v_lshlrev_b32_e32 v0, 4, v0
	v_or_b32_e32 v2, v1, v0
	v_or_b32_e32 v110, 0x14000, v2
	v_mov_b32_e32 v92, 0
	v_mov_b32_e32 v93, v92
	v_mov_b32_e32 v94, v92
	v_mov_b32_e32 v95, v92
	v_mov_b32_e32 v88, v92
	v_mov_b32_e32 v89, v92
	v_mov_b32_e32 v90, v92
	v_mov_b32_e32 v91, v92
	v_mov_b32_e32 v84, v92
	v_mov_b32_e32 v85, v92
	v_mov_b32_e32 v86, v92
	v_mov_b32_e32 v87, v92
	v_mov_b32_e32 v72, v92
	v_mov_b32_e32 v73, v92
	v_mov_b32_e32 v74, v92
	v_mov_b32_e32 v75, v92
	v_mov_b32_e32 v60, v92
	v_mov_b32_e32 v61, v92
	v_mov_b32_e32 v62, v92
	v_mov_b32_e32 v63, v92
	v_mov_b32_e32 v44, v92
	v_mov_b32_e32 v45, v92
	v_mov_b32_e32 v46, v92
	v_mov_b32_e32 v47, v92
	v_mov_b32_e32 v36, v92
	v_mov_b32_e32 v37, v92
	v_mov_b32_e32 v38, v92
	v_mov_b32_e32 v39, v92
	v_mov_b32_e32 v32, v92
	v_mov_b32_e32 v33, v92
	v_mov_b32_e32 v34, v92
	v_mov_b32_e32 v35, v92
	v_mov_b32_e32 v28, v92
	v_mov_b32_e32 v29, v92
	v_mov_b32_e32 v30, v92
	v_mov_b32_e32 v31, v92
	v_mov_b32_e32 v24, v92
	v_mov_b32_e32 v25, v92
	v_mov_b32_e32 v26, v92
	v_mov_b32_e32 v27, v92
	v_mov_b32_e32 v20, v92
	v_mov_b32_e32 v21, v92
	v_mov_b32_e32 v22, v92
	v_mov_b32_e32 v23, v92
	v_mov_b32_e32 v12, v92
	v_mov_b32_e32 v13, v92
	v_mov_b32_e32 v14, v92
	v_mov_b32_e32 v15, v92
	v_mov_b32_e32 v8, v92
	v_mov_b32_e32 v9, v92
	v_mov_b32_e32 v10, v92
	v_mov_b32_e32 v11, v92
	v_mov_b32_e32 v4, v92
	v_mov_b32_e32 v5, v92
	v_mov_b32_e32 v6, v92
	v_mov_b32_e32 v7, v92
	s_mov_b32 s4, 0x14040
	s_waitcnt vmcnt(4) lgkmcnt(0)
	s_barrier
	ds_read_b128 v[40:43], v110
	v_bitop3_b32 v111, v1, s4, v0 bitop3:0x36
	ds_read_b128 v[48:51], v110 offset:2048
	v_lshlrev_b32_e32 v0, 7, v98
	v_bitop3_b32 v1, v98, v99, 6 bitop3:0x6c
	v_add_u32_e32 v109, 51, v98
	v_lshl_or_b32 v113, v1, 4, v0
	ds_read_b128 v[56:59], v113
	ds_read_b128 v[52:55], v113 offset:2048
	v_lshlrev_b32_e32 v0, 7, v109
	v_bitop3_b32 v1, v109, v99, 6 bitop3:0x6c
	v_lshl_or_b32 v114, v1, 4, v0
	ds_read_b128 v[64:67], v114
	ds_read_b128 v[68:71], v114 offset:2048
	ds_read_b128 v[76:79], v110 offset:4096
	ds_read_b128 v[80:83], v110 offset:6144
	s_lshr_b32 s10, s34, 7
	s_mul_i32 s12, s33, 0x64
	v_lshl_add_u64 v[100:101], v[18:19], 1, s[22:23]
	s_mov_b32 s5, 0
	s_mov_b32 s13, 0xc000
	s_mov_b64 s[8:9], 0x400
	v_mov_b32_e32 v112, 0x64
	s_mov_b32 s14, 0
	v_mov_b32_e32 v16, v92
	v_mov_b32_e32 v17, v92
	v_mov_b32_e32 v18, v92
	v_mov_b32_e32 v19, v92
	v_mov_b32_e32 v0, v92
	v_mov_b32_e32 v1, v92
	v_mov_b32_e32 v2, v92
	v_mov_b32_e32 v3, v92
	s_mov_b32 s40, 1
	s_mov_b32 s41, 1
	v_mov_b32_e32 v115, v111
	s_add_i32 s4, s12, 3
	s_lshl_b32 s4, s4, 14
	v_lshl_add_u64 v[148:149], v[100:101], 0, s[4:5]
	s_add_i32 s42, s27, 0xc000
	v_lshl_add_u64 v[150:151], v[148:149], 0, s[8:9]
	s_mov_b32 s45, 0
	s_waitcnt lgkmcnt(0)
